# cfox queue first in PREP, fp8 gate-GEMM unit rebalance across CUs
# speedup vs baseline: 1.0160x; 1.0037x over previous
.LBB0_168:
	s_add_i32 s51, s51, 1
	s_mul_i32 s13, s51, s29
	s_mul_hi_u32 s15, s51, s28
	s_add_i32 s15, s15, s13
	s_mul_i32 s13, s51, s28
	s_add_u32 s16, s13, s2
	s_addc_u32 s17, s15, s3
	s_cmp_lg_u32 s28, 0x100
	s_cbranch_scc1 .Lin_rebal_skip
	s_cmp_eq_u32 s51, 7
	s_cselect_b32 s100, 64, 0
	s_cmp_lt_u32 s2, s100
	s_cselect_b32 s16, 0x800, s16
	s_sub_u32 s100, s2, 64
	s_cmp_lt_u32 s100, 64
	s_cselect_b32 s101, 8, -1
	s_add_u32 s100, s100, 0x700
	s_cmp_eq_u32 s51, s101
	s_cselect_b32 s16, s100, s16
	s_cselect_b32 s17, 0, s17
.Lin_rebal_skip:
	v_mov_b64_e32 v[4:5], 0x800
	v_cmp_lt_i64_e64 s[36:37], s[16:17], v[4:5]
	v_mov_b64_e32 v[4:5], 0x7ff
	v_cmp_gt_i64_e32 vcc, s[16:17], v[4:5]
	s_cbranch_vccnz .LBB0_174
	s_ashr_i32 s12, s16, 31
	s_lshr_b32 s12, s12, 29
	s_add_i32 s14, s16, s12
	s_and_b32 s12, s14, -8
	s_sub_i32 s15, s16, s12
	s_cmp_gt_i32 s15, -1
	s_mov_b64 s[12:13], -1
	s_cbranch_scc0 .LBB0_171
	s_lshl_b32 s16, s15, 8
	s_mov_b64 s[12:13], 0

.LBB0_252:
	s_cmp_le_i32 s90, s16
	s_cselect_b64 s[0:1], -1, 0
	s_cmp_lt_i32 s16, s91
	s_cselect_b64 s[2:3], -1, 0
	s_and_b64 s[2:3], s[0:1], s[2:3]
	v_mov_b32_e32 v1, v0
	s_andn2_b64 vcc, exec, s[2:3]
	s_cbranch_vccnz .LBB0_425
	v_writelane_b32 v255, s2, 5
	v_writelane_b32 v255, s3, 6
	v_readlane_b32 s18, v253, 24
	s_movk_i32 s24, 0x7200
	s_mov_b32 s25, 0x800000
	s_mov_b32 s19, 0
	s_nop 0
	s_lshl_b32 s22, s18, 2
	s_lshl_b32 s18, s18, 12
	s_branch .LBB0_393
.Lprep_after_cfox:
	v_readlane_b32 s2, v255, 5
	v_readlane_b32 s3, v255, 6
	v_mov_b32_e32 v1, v0
	s_nop 3
	v_writelane_b32 v253, s2, 27
	s_add_i32 s23, s72, 0x21000
	s_movk_i32 s45, 0x7200
	v_writelane_b32 v253, s3, 28
	v_writelane_b32 v253, s84, 29
	s_mov_b32 s43, 0x800000
	v_readlane_b32 s73, v252, 0
	v_writelane_b32 v253, s85, 30
	v_writelane_b32 v253, s86, 31
	v_writelane_b32 v253, s87, 32
	v_cmp_eq_u32_e64 s[36:37], 0, v1
	v_readlane_b32 s0, v253, 17
	v_readlane_b32 s1, v253, 18
	s_mov_b32 s5, s1
	v_readlane_b32 s0, v253, 24
	s_lshl_b32 s4, s0, 10
	v_readlane_b32 s2, v253, 19
	s_lshl_b64 s[8:9], s[4:5], 2
	v_readlane_b32 s1, v253, 25
	s_mov_b32 s2, s0
	s_add_u32 s0, s68, s8
	v_readlane_b32 s3, v253, 20
	v_writelane_b32 v253, s8, 33
	s_addc_u32 s1, s69, s9
	s_mul_i32 s10, s2, 0x6000
	v_writelane_b32 v253, s9, 34
	s_add_u32 s8, s0, 0x10000
	s_addc_u32 s9, s1, 0
	s_mov_b32 s1, s5
	s_lshl_b32 s22, s2, 2
	v_writelane_b32 v253, s0, 17
	s_mov_b64 s[6:7], s[68:69]
	s_add_i32 s24, s72, 0x10100
	v_writelane_b32 v253, s1, 18
	v_writelane_b32 v253, s2, 19
	v_writelane_b32 v253, s3, 20
	s_add_i32 s1, s72, 0x1cf08
	v_writelane_b32 v253, s1, 35
	s_add_i32 s1, s72, 0x1cf10
	v_writelane_b32 v253, s1, 36
	s_add_i32 s1, s72, 0x1cf18
	v_writelane_b32 v253, s1, 37
	s_add_i32 s1, s72, 0x1cf20
	v_writelane_b32 v253, s1, 39
	s_add_i32 s1, s72, 0x1cf28
	v_writelane_b32 v253, s1, 41
	s_add_i32 s1, s72, 0x1cf30
	v_writelane_b32 v253, s1, 43
	s_add_i32 s1, s72, 0x1cf38
	v_writelane_b32 v253, s1, 45
	s_add_i32 s1, s72, 0x1cf40
	v_writelane_b32 v253, s1, 47
	s_add_i32 s1, s72, 0x1cf48
	v_writelane_b32 v253, s1, 49
	s_add_i32 s1, s72, 0x1cf50
	s_mov_b32 s0, s72
	v_writelane_b32 v253, s1, 51
	s_add_i32 s1, s72, 0x1cf58
	s_add_i32 s25, s72, 0x14500
	s_add_i32 s26, s72, 0x18900
	s_add_i32 s27, s72, 0x1cd00
	s_add_i32 s28, s72, 0x1ce00
	s_add_i32 s29, s72, 0x1cf00
	s_add_i32 s30, s72, 0x21080
	s_add_i32 s31, s72, 0x21078
	s_mov_b32 s11, s5
	s_add_i32 s41, s72, 0x1cefc
	s_add_i32 s34, s72, 0x1cd08
	s_add_i32 s49, s72, 0x1cd10
	s_add_i32 s40, s72, 0x1cd18
	s_add_i32 s42, s72, 0x1cd20
	s_add_i32 s53, s72, 0x1cd28
	s_add_i32 s55, s72, 0x1cd30
	s_add_i32 s48, s72, 0x1cd38
	s_add_i32 s50, s72, 0x1cd40
	s_add_i32 s52, s72, 0x1cd48
	s_add_i32 s54, s72, 0x1cd50
	s_add_i32 s56, s72, 0x1cd58
	v_writelane_b32 v253, s1, 53
	s_add_i32 s58, s72, 0x1cd60
	s_add_i32 s59, s72, 0x1cf60
	s_add_i32 s60, s72, 0x1cd68
	s_add_i32 s61, s72, 0x1cf68
	s_add_i32 s62, s72, 0x1cd70
	s_add_i32 s63, s72, 0x1cf70
	s_add_i32 s64, s72, 0x1cd78
	s_add_i32 s65, s72, 0x1cf78
	s_add_i32 s66, s72, 0x1cd80
	s_add_i32 s67, s72, 0x1cf80
	s_add_i32 s68, s72, 0x1cd88
	s_add_i32 s69, s72, 0x1cf88
	s_add_i32 s72, s72, 0x1cd90
	s_add_i32 s51, s0, 0x1cf90
	s_add_i32 s74, s0, 0x1cd98
	s_add_i32 s57, s0, 0x1cf98
	s_add_i32 s76, s0, 0x1cda0
	s_add_i32 s77, s0, 0x1cfa0
	s_add_i32 s78, s0, 0x1cda8
	s_add_i32 s79, s0, 0x1cfa8
	s_add_i32 s80, s0, 0x1cdb0
	s_add_i32 s81, s0, 0x1cfb0
	s_add_i32 s82, s0, 0x1cdb8
	s_add_i32 s83, s0, 0x1cfb8
	s_add_i32 s84, s0, 0x1cdc0
	s_add_i32 s85, s0, 0x1cfc0
	s_add_i32 s86, s0, 0x1cdc8
	s_add_i32 s87, s0, 0x1cfc8
	s_add_i32 s88, s0, 0x1cdd0
	s_add_i32 s89, s0, 0x1cfd0
	s_add_i32 s90, s0, 0x1cdd8
	s_add_i32 s91, s0, 0x1cfd8
	s_add_i32 s92, s0, 0x1cde0
	s_add_i32 s93, s0, 0x1cfe0
	s_add_i32 s94, s0, 0x1cde8
	s_add_i32 s95, s0, 0x1cfe8
	s_add_i32 s96, s0, 0x1cdf0
	s_add_i32 s97, s0, 0x1cff0
	s_add_i32 s2, s0, 0x1cdf8
	s_mov_b32 s33, s0
	s_add_i32 s3, s0, 0x1cff8
	s_branch .LBB0_257
